# computing workgroups convert the last 3x171 runs of expert tiles after attn_norm (4-slot converter instance), 85 converters stop earlier; on top of vm10+womap+nop
# speedup vs baseline: 1.0177x; 1.0177x over previous
; #define LDS_AS __attribute__((address_space(3)))
; #define OPAQUE_TID(P) (((P).wid0 << 6) | lane_id_now())
; template <int NS, bool STREAM_ONLY = false>
; DI void convert_experts_dma(const Params& p, LDS_AS unsigned char* lds, int bid, int nb) {
;   const int tid = OPAQUE_TID(p), wid = __builtin_amdgcn_readfirstlane(tid >> 6), lane = tid & 63;
;   constexpr int NT = 32 * 1536;
;   const int nvalid = bid < NT / CVG ? CVG * ((NT / CVG - bid + nb - 1) / nb) : 0;
; __global__ void __launch_bounds__(NTHREADS, 2) k_forward(Params p_in) {
;     ...
;     if (ncv == 0) convert_experts_dma<4>(p, lds, bid, nb);
.LBB0_1119:
	s_or_b64 exec, exec, s[0:1]
	s_mov_b64 s[12:13], 0
	s_mov_b32 s20, 0
	s_mov_b64 s[0:1], 0
	v_readlane_b32 s97, v255, 13
	s_mov_b32 s99, s96
	s_nop 0
	s_mov_b32 s98, s97
	s_cmp_lg_u32 s55, 0
	s_cbranch_scc0 .LBB0_1181
	v_readlane_b32 s98, v255, 17
	s_sub_i32 s99, s96, s55
	s_add_i32 s98, s98, 0x2dff
	s_branch .LBB0_1181
.LBB0_1121:
	v_mov_b32_e32 v0, 0
	ds_read_b32 v2, v0
	ds_read_b32 v3, v0 offset:4
	s_waitcnt lgkmcnt(0)
	s_barrier
	v_mbcnt_lo_u32_b32 v0, -1, 0
	v_mbcnt_hi_u32_b32 v0, -1, v0
	s_mov_b32 s6, 0
	v_or_b32_e32 v1, s87, v0
	s_cmpk_gt_i32 s54, 0x2dfe
	v_readfirstlane_b32 s0, v1
	s_mov_b32 s18, 0
	s_cbranch_scc1 .LBB0_1123
	s_abs_i32 s1, s55
	v_cvt_f32_u32_e32 v1, s1
	s_sub_i32 s2, s55, s54
	s_add_i32 s3, s2, 0x2dfe
	s_sub_i32 s2, 0xffffd202, s2
	v_rcp_iflag_f32_e32 v1, v1
	s_xor_b32 s5, s3, s55
	s_sub_i32 s4, 0, s1
	s_max_i32 s2, s3, s2
	v_mul_f32_e32 v1, 0x4f7ffffe, v1
	v_cvt_u32_f32_e32 v1, v1
	s_ashr_i32 s3, s5, 31
	v_readfirstlane_b32 s5, v1
	s_mul_i32 s4, s4, s5
	s_mul_hi_u32 s4, s5, s4
	s_add_i32 s5, s5, s4
	s_mul_hi_u32 s4, s2, s5
	s_mul_i32 s5, s4, s1
	s_sub_i32 s2, s2, s5
	s_add_i32 s7, s4, 1
	s_sub_i32 s5, s2, s1
	s_cmp_ge_u32 s2, s1
	s_cselect_b32 s4, s7, s4
	s_cselect_b32 s2, s5, s2
	s_add_i32 s5, s4, 1
	s_cmp_ge_u32 s2, s1
	s_cselect_b32 s1, s5, s4
	s_xor_b32 s1, s1, s3
	s_sub_i32 s1, s1, s3
	s_lshl_b32 s18, s1, 2

; #define LDS_AS __attribute__((address_space(3)))
; #define OPAQUE_TID(P) (((P).wid0 << 6) | lane_id_now())
; template <int NS, bool STREAM_ONLY = false>
; DI void convert_experts_dma(const Params& p, LDS_AS unsigned char* lds, int bid, int nb) {
;   const int tid = OPAQUE_TID(p), wid = __builtin_amdgcn_readfirstlane(tid >> 6), lane = tid & 63;
;   constexpr int NT = 32 * 1536;
;   const int nvalid = bid < NT / CVG ? CVG * ((NT / CVG - bid + nb - 1) / nb) : 0;
;     ...
;   const __amdgpu_buffer_rsrc_t rs1 = __builtin_amdgcn_make_buffer_rsrc((void*)p.w_gate_up, 0, 0x40000000u, 0x00020000);
;   const __amdgpu_buffer_rsrc_t rs2 = __builtin_amdgcn_make_buffer_rsrc((void*)p.w_down, 0, 0x20000000u, 0x00020000);
;   const __amdgpu_buffer_rsrc_t rs0 = __builtin_amdgcn_make_buffer_rsrc((void*)p.w_down, 0, 0u, 0x00020000);
;   const unsigned vo1 = ((unsigned)lane >> 4) * 16384u + ((((unsigned)lane & 15u) ^ (unsigned)wid) << 4);
;   const unsigned vo2 = ((unsigned)lane >> 4) * 8192u + ((((unsigned)lane & 15u) ^ (unsigned)wid) << 4);
;   const unsigned ldsw = (unsigned)__builtin_amdgcn_readfirstlane((int)(unsigned)(size_t)lds) + (unsigned)wid * 4096u;
;   const int n = 8 * wid + (lane >> 3), kc = lane & 7;
;   const unsigned roff = (unsigned)kc * 4096u + ((((unsigned)n >> 2) ^ (unsigned)kc) << 4) + (((unsigned)n & 3u) << 2);
;     ...
;   CVD_ISSUE(0, 0); CVD_ISSUE(1, 1); CVD_ISSUE(2, 2);
.LBB0_1181:
	v_mbcnt_lo_u32_b32 v0, -1, 0
	v_mbcnt_hi_u32_b32 v0, -1, v0
	s_cmpk_gt_i32 s98, 0x2fff
	v_or_b32_e32 v1, s87, v0
	s_nop 0
	v_readfirstlane_b32 s0, v1
	s_cbranch_scc1 .LBB0_1183
	s_abs_i32 s1, s99
	v_cvt_f32_u32_e32 v1, s1
	s_sub_i32 s2, s99, s98
	s_add_i32 s3, s2, 0x2fff
	s_sub_i32 s2, 0xffffd001, s2
	v_rcp_iflag_f32_e32 v1, v1
	s_xor_b32 s5, s3, s99
	s_sub_i32 s4, 0, s1
	s_max_i32 s2, s3, s2
	v_mul_f32_e32 v1, 0x4f7ffffe, v1
	v_cvt_u32_f32_e32 v1, v1
	s_ashr_i32 s3, s5, 31
	v_readfirstlane_b32 s5, v1
	s_mul_i32 s4, s4, s5
	s_mul_hi_u32 s4, s5, s4
	s_add_i32 s5, s5, s4
	s_mul_hi_u32 s4, s2, s5
	s_mul_i32 s5, s4, s1
	s_sub_i32 s2, s2, s5
	s_add_i32 s6, s4, 1
	s_sub_i32 s5, s2, s1
	s_cmp_ge_u32 s2, s1
	s_cselect_b32 s4, s6, s4
	s_cselect_b32 s2, s5, s2
	s_add_i32 s5, s4, 1
	s_cmp_ge_u32 s2, s1
	s_cselect_b32 s1, s5, s4
	s_xor_b32 s1, s1, s3
	s_sub_i32 s1, s1, s3
	s_lshl_b32 s20, s1, 2
.LBB0_1183:
	s_ashr_i32 s23, s0, 6
	v_readlane_b32 s24, v254, 6
	s_lshl_b32 s0, s23, 12
	v_readlane_b32 s25, v254, 7
	v_readlane_b32 s29, v254, 11
	s_add_i32 s24, s0, 0
	s_and_b32 s9, s25, 0xffff
	s_and_b32 s5, s29, 0xffff
	s_add_i32 s21, s24, 16
	s_lshl_b32 s25, s98, 2
	v_bfe_u32 v1, v0, 4, 2
	s_cmp_gt_i32 s20, 0
	v_lshlrev_b32_e32 v2, 14, v1
	v_bitop3_b32 v3, s23, v0, 15 bitop3:0x78
	s_cselect_b64 s[14:15], -1, 0
	s_cmpk_gt_i32 s25, 0x3fff
	v_readlane_b32 s28, v254, 10
	v_lshl_add_u32 v2, v3, 4, v2
	v_lshlrev_b32_e32 v1, 13, v1
	s_cselect_b64 s[0:1], -1, 0
	s_cmpk_lt_i32 s25, 0x4000
	s_mov_b32 s7, 0x20000
	s_mov_b32 s10, 2.0
	s_brev_b32 s2, 4
	s_mov_b32 s4, s28
	s_mov_b32 s6, 0
	v_sub_u32_e32 v3, v2, v1
	s_cselect_b64 s[16:17], -1, 0
	s_mov_b64 s[18:19], -1
	s_and_b64 vcc, exec, s[14:15]
	v_readlane_b32 s26, v254, 8
	v_readlane_b32 s27, v254, 9
	v_readlane_b32 s30, v254, 12
	v_readlane_b32 s31, v254, 13
	s_cbranch_vccnz .LBB0_1185
	v_cndmask_b32_e64 v1, v3, v2, s[0:1]
	s_mov_b32 m0, s21
	s_nop 0
	buffer_load_dwordx4 v1, s[4:7], s6 offen lds
	s_add_i32 s3, s24, 0x410
	s_mov_b32 m0, s3
	s_nop 0
	buffer_load_dwordx4 v1, s[4:7], s6 offen lds
	s_add_i32 s3, s24, 0x810
	s_mov_b32 m0, s3
	s_nop 0
	buffer_load_dwordx4 v1, s[4:7], s6 offen lds
	s_add_i32 s3, s24, 0xc10
	s_mov_b32 m0, s3
	s_nop 0
	buffer_load_dwordx4 v1, s[4:7], s6 offen lds
	s_mov_b64 s[18:19], 0

; template <int NS, bool STREAM_ONLY = false>
; DI void convert_experts_dma(const Params& p, LDS_AS unsigned char* lds, int bid, int nb) {
;     ...
;   for (int i = 0; i < nvalid; ++i) {
;     if (NS == 4) asm volatile("s_waitcnt vmcnt(8)" ::: "memory");
;     else asm volatile("s_waitcnt vmcnt(12)" ::: "memory");
;     __builtin_amdgcn_s_barrier();
;     __builtin_amdgcn_sched_barrier(0);
;     const int sp = si == 0 ? NS - 1 : si - 1;
;     CVD_ISSUE(i + NS - 1, sp);
.LBB0_1207:
	s_waitcnt vmcnt(8)
	s_barrier
	s_add_i32 s8, s24, 3
	s_lshr_b32 s0, s8, 2
	s_mul_i32 s0, s0, s99
	s_add_i32 s0, s0, s98
	s_lshl_b32 s0, s0, 2
	s_and_b32 s1, s8, 3
	s_or_b32 s3, s0, s1
	s_cmpk_gt_i32 s3, 0x3fff
	s_cselect_b64 s[0:1], -1, 0
	s_cmpk_lt_i32 s3, 0x4000
	s_cselect_b64 s[16:17], -1, 0
	s_lshl_b32 s25, s23, 15
	s_add_i32 s11, s25, 0xffff8000
	s_cmp_lg_u32 s23, 0
	s_cselect_b32 s11, s11, 0x18000
	s_add_i32 s14, s11, s21
	s_cmp_lt_i32 s8, s20
	s_mov_b64 s[18:19], -1
	s_cbranch_scc1 .LBB0_1209
	v_cndmask_b32_e64 v6, v3, v2, s[0:1]
	s_mov_b32 m0, s14
	s_nop 0
	buffer_load_dwordx4 v6, s[4:7], s15 offen lds
	s_add_i32 s8, s14, 0x400
	s_mov_b32 m0, s8
	s_nop 0
	buffer_load_dwordx4 v6, s[4:7], s15 offen lds
	s_add_i32 s8, s14, 0x800
	s_mov_b32 m0, s8
	s_nop 0
	buffer_load_dwordx4 v6, s[4:7], s15 offen lds
	s_add_i32 s8, s14, 0xc00
	s_mov_b32 m0, s8
	s_nop 0
	buffer_load_dwordx4 v6, s[4:7], s15 offen lds
	s_mov_b64 s[18:19], 0

; template <int NS, bool STREAM_ONLY = false>
; DI void convert_experts_dma(const Params& p, LDS_AS unsigned char* lds, int bid, int nb) {
;     ...
;     const int t = __builtin_amdgcn_readfirstlane(CVX_TILE_OF(i));
;     const int e = CVX_E(t), r = CVX_R(t); const bool gu = r < 1024;
;     const int kt = gu ? (r >> 6) : ((r - 1024) >> 5), ntile = gu ? (r & 63) : ((r - 1024) & 31);
;     unsigned char* Wq = gu ? p.wq1 + (size_t)e * 4096 * 2048 : p.wq2 + (size_t)e * 2048 * 2048;
.LBB0_1214:
	s_lshr_b32 s0, s24, 2
	s_mul_i32 s0, s0, s99
	s_add_i32 s0, s0, s98
	s_lshl_b32 s0, s0, 2
	s_and_b32 s1, s24, 3
	s_or_b32 s3, s0, s1
	s_cmpk_gt_i32 s3, 0x3fff
	s_cselect_b64 s[16:17], -1, 0
	s_cmpk_lt_i32 s3, 0x4000
	s_mov_b64 s[18:19], -1
	s_cbranch_scc0 .LBB0_1216
	s_ashr_i32 s0, s3, 9
	s_ashr_i32 s1, s0, 31
	s_lshl_b64 s[0:1], s[0:1], 22
	s_add_u32 s0, s52, s0
	s_addc_u32 s1, s53, s1
	s_mov_b64 s[18:19], 0
